# converter: s_sleep 30 throttle + nt on its read-once f32 weight loads and fp8 stores
# speedup vs baseline: 1.0179x; 1.0179x over previous
; #define P0S_LOAD(dst, krow0) do { _Pragma("unroll") for (int i = 0; i < 16; ++i) dst[i] = *(const f32x4*)(wp + (size_t)((krow0) + 2 * i) * ld); } while (0)
; #define P0S_PUT(src, r0) do { _Pragma("unroll") for (int i = 0; i < 16; ++i) { \
;         u32x2 pk; pk.x = cvtpk(src[i][0], src[i][1]) + 0x02800280u; pk.y = cvtpk(src[i][2], src[i][3]) + 0x02800280u;        \
;         *(LAS u32x2*)(img + wb[i & 7] + ((r0) / 16 + (i >> 3)) * 4096) = pk; } } while (0)
; template <int MODE>
; DI void p0_strip_fp8(const float* W, int ld, unsigned char* WT, int K, int n0, LAS unsigned char* img, int lane) {
;     ...
;     for (int nb = 0; nb < 8; ++nb) { const int n = n0 + 16 * nb + i16; int row = n; if (MODE == 1) { const int ff = n >> 1; row = 256 * (ff >> 7) + 128 * (n & 1) + (ff & 127); } orow[nb] = row * K + 16 * g; }
;     f32x4 va[16], vb[16];
;     ...
;     P0S_LOAD(va, 0);
; #pragma unroll 1
;     for (int kb = 0; kb < 32; ++kb) {
;         P0S_LOAD(vb, 64 * kb + 32);
;         P0S_PUT(va, 0);
;         if (kb < 31) P0S_LOAD(va, 64 * kb + 64);
;         P0S_PUT(vb, 32);
; DI void p0_expert_weights(Frame& F, int wk, int nwk) {
;     ...
;         else { const int r = cx - C_UP, e = r >> 4, nb = r & 15; p0_strip_fp8<0>(F.w_down + (size_t)e * FF * DM, DM, F.ws + WS_WDN + (size_t)e * DM * FF, FF, 128 * nb, img, F.lane); }
.LBB0_276:
	s_cmpk_gt_i32 s8, 0x3ff
	s_cselect_b64 s[4:5], -1, 0
	s_lshl_b32 s61, s8, 7
	s_mov_b64 s[0:1], -1
	s_and_b64 vcc, exec, s[4:5]
	s_cbranch_vccz .LBB0_284
	s_add_i32 s0, s8, 0xfffffc00
	s_lshr_b32 s2, s0, 4
	s_lshl_b64 s[0:1], s[2:3], 22
	s_add_u32 s0, s9, s0
	s_addc_u32 s1, s10, s1
	s_and_b32 s62, s61, 0x780
	s_lshl_b64 s[6:7], s[2:3], 24
	v_lshl_add_u64 v[2:3], v[140:141], 0, s[6:7]
	s_lshl_b32 s2, s62, 2
	v_lshl_add_u64 v[2:3], v[2:3], 0, s[2:3]
	v_lshl_add_u64 v[144:145], v[2:3], 0, v[138:139]
	v_add_co_u32_e32 v2, vcc, s22, v144
	v_or_b32_e32 v1, s62, v9
	s_nop 0
	v_addc_co_u32_e32 v3, vcc, 0, v145, vcc
	global_load_dwordx4 v[10:13], v[144:145], off nt
	global_load_dwordx4 v[14:17], v[2:3], off nt
	v_add_co_u32_e32 v2, vcc, s15, v144
	s_mov_b32 s62, 0
	s_nop 0
	v_addc_co_u32_e32 v3, vcc, 0, v145, vcc
	v_add_co_u32_e32 v4, vcc, s23, v144
	s_nop 1
	v_addc_co_u32_e32 v5, vcc, 0, v145, vcc
	global_load_dwordx4 v[18:21], v[2:3], off nt
	global_load_dwordx4 v[22:25], v[4:5], off nt
	v_add_co_u32_e32 v2, vcc, s16, v144
	s_nop 1
	v_addc_co_u32_e32 v3, vcc, 0, v145, vcc
	v_add_co_u32_e32 v4, vcc, s24, v144
	s_nop 1
	v_addc_co_u32_e32 v5, vcc, 0, v145, vcc
	global_load_dwordx4 v[26:29], v[2:3], off nt
	global_load_dwordx4 v[30:33], v[4:5], off nt
	v_add_co_u32_e32 v2, vcc, s17, v144
	s_nop 1
	v_addc_co_u32_e32 v3, vcc, 0, v145, vcc
	v_add_co_u32_e32 v4, vcc, s25, v144
	s_nop 1
	v_addc_co_u32_e32 v5, vcc, 0, v145, vcc
	global_load_dwordx4 v[34:37], v[2:3], off nt
	global_load_dwordx4 v[38:41], v[4:5], off nt
	v_add_co_u32_e32 v2, vcc, s18, v144
	s_nop 1
	v_addc_co_u32_e32 v3, vcc, 0, v145, vcc
	v_add_co_u32_e32 v4, vcc, s26, v144
	s_nop 1
	v_addc_co_u32_e32 v5, vcc, 0, v145, vcc
	global_load_dwordx4 v[42:45], v[2:3], off nt
	global_load_dwordx4 v[46:49], v[4:5], off nt
	v_add_co_u32_e32 v2, vcc, s19, v144
	s_nop 1
	v_addc_co_u32_e32 v3, vcc, 0, v145, vcc
	v_add_co_u32_e32 v4, vcc, 0x2c000, v144
	s_nop 1
	v_addc_co_u32_e32 v5, vcc, 0, v145, vcc
	global_load_dwordx4 v[50:53], v[2:3], off nt
	global_load_dwordx4 v[54:57], v[4:5], off nt
	v_add_co_u32_e32 v2, vcc, s20, v144
	s_nop 1
	v_addc_co_u32_e32 v3, vcc, 0, v145, vcc
	v_add_co_u32_e32 v4, vcc, 0x34000, v144
	s_nop 1
	v_addc_co_u32_e32 v5, vcc, 0, v145, vcc
	global_load_dwordx4 v[58:61], v[2:3], off nt
	global_load_dwordx4 v[62:65], v[4:5], off nt
	v_add_co_u32_e32 v2, vcc, 0x38000, v144
	s_nop 1
	v_addc_co_u32_e32 v3, vcc, 0, v145, vcc
	v_add_co_u32_e32 v4, vcc, 0x3c000, v144
	s_nop 1
	v_addc_co_u32_e32 v5, vcc, 0, v145, vcc
	global_load_dwordx4 v[66:69], v[2:3], off nt
	global_load_dwordx4 v[70:73], v[4:5], off nt
	v_lshl_or_b32 v2, v1, 11, v149
	v_or_b32_e32 v1, 0x8000, v2
	v_or_b32_e32 v4, 0x10000, v2
	v_or_b32_e32 v3, 0x18000, v2
	v_or_b32_e32 v6, 0x20000, v2
	v_or_b32_e32 v5, 0x28000, v2
	v_or_b32_e32 v8, 0x30000, v2
	v_or_b32_e32 v7, 0x38000, v2
.LBB0_278:
	s_lshl_b32 s2, s62, 17
	v_lshl_add_u64 v[146:147], s[2:3], 2, v[144:145]
	s_waitcnt vmcnt(26)
	v_add_co_u32_e32 v74, vcc, s27, v146
	s_waitcnt vmcnt(15)
	v_cvt_pk_bf16_f32 v164, v10, v11
	v_addc_co_u32_e32 v75, vcc, 0, v147, vcc
	v_add_co_u32_e32 v76, vcc, s28, v146
	v_add_u32_e32 v172, 0x2800280, v164
	s_nop 0
	v_addc_co_u32_e32 v77, vcc, 0, v147, vcc
	global_load_dwordx4 v[134:137], v[74:75], off nt
	global_load_dwordx4 v[118:121], v[76:77], off nt
	v_add_co_u32_e32 v74, vcc, s29, v146
	v_cvt_pk_bf16_f32 v164, v12, v13
	s_nop 0
	v_addc_co_u32_e32 v75, vcc, 0, v147, vcc
	v_add_co_u32_e32 v76, vcc, s30, v146
	s_waitcnt vmcnt(9)
	v_cvt_pk_bf16_f32 v188, v42, v43
	v_addc_co_u32_e32 v77, vcc, 0, v147, vcc
	global_load_dwordx4 v[130:133], v[74:75], off nt
	global_load_dwordx4 v[110:113], v[76:77], off nt
	v_add_co_u32_e32 v74, vcc, s31, v146
	v_cvt_pk_bf16_f32 v189, v44, v45
	s_nop 0
	v_addc_co_u32_e32 v75, vcc, 0, v147, vcc
	v_add_co_u32_e32 v76, vcc, s33, v146
	v_add_u32_e32 v173, 0x2800280, v164
	s_nop 0
	v_addc_co_u32_e32 v77, vcc, 0, v147, vcc
	global_load_dwordx4 v[126:129], v[74:75], off nt
	global_load_dwordx4 v[106:109], v[76:77], off nt
	v_add_co_u32_e32 v74, vcc, s34, v146
	v_add_u32_e32 v164, v154, v148
	s_nop 0
	v_addc_co_u32_e32 v75, vcc, 0, v147, vcc
	v_add_co_u32_e32 v76, vcc, s35, v146
	v_cvt_pk_bf16_f32 v165, v14, v15
	s_nop 0
	v_addc_co_u32_e32 v77, vcc, 0, v147, vcc
	global_load_dwordx4 v[122:125], v[74:75], off nt
	global_load_dwordx4 v[102:105], v[76:77], off nt
	v_add_co_u32_e32 v74, vcc, s36, v146
	v_add_u32_e32 v188, 0x2800280, v188
	s_nop 0
	v_addc_co_u32_e32 v75, vcc, 0, v147, vcc
	v_add_co_u32_e32 v76, vcc, s37, v146
	v_add_u32_e32 v189, 0x2800280, v189
	s_nop 0
	v_addc_co_u32_e32 v77, vcc, 0, v147, vcc
	global_load_dwordx4 v[114:117], v[74:75], off nt
	global_load_dwordx4 v[94:97], v[76:77], off nt
	v_add_co_u32_e32 v74, vcc, s38, v146
	v_add_u32_e32 v174, 0x2800280, v165
	s_nop 0
	v_addc_co_u32_e32 v75, vcc, 0, v147, vcc
	v_add_co_u32_e32 v76, vcc, s39, v146
	v_cvt_pk_bf16_f32 v165, v16, v17
	s_nop 0
	v_addc_co_u32_e32 v77, vcc, 0, v147, vcc
	global_load_dwordx4 v[98:101], v[74:75], off nt
	global_load_dwordx4 v[86:89], v[76:77], off nt
	v_add_co_u32_e32 v74, vcc, s40, v146
	v_add_u32_e32 v175, 0x2800280, v165
	s_nop 0
	v_addc_co_u32_e32 v75, vcc, 0, v147, vcc
	v_add_co_u32_e32 v76, vcc, s41, v146
	v_add_u32_e32 v165, v155, v148
	s_nop 0
	v_addc_co_u32_e32 v77, vcc, 0, v147, vcc
	global_load_dwordx4 v[90:93], v[74:75], off nt
	global_load_dwordx4 v[78:81], v[76:77], off nt
	v_add_co_u32_e32 v74, vcc, s42, v146
	v_cvt_pk_bf16_f32 v166, v18, v19
	s_nop 0
	v_addc_co_u32_e32 v75, vcc, 0, v147, vcc
	v_add_co_u32_e32 v76, vcc, s43, v146
	v_add_u32_e32 v176, 0x2800280, v166
	s_nop 0
	v_addc_co_u32_e32 v77, vcc, 0, v147, vcc
	global_load_dwordx4 v[82:85], v[74:75], off nt
	s_nop 0
	global_load_dwordx4 v[74:77], v[76:77], off nt
	ds_write2st64_b64 v164, v[172:173], v[188:189] offset1:8
	s_waitcnt vmcnt(22)
; #define P0S_LOAD(dst, krow0) do { _Pragma("unroll") for (int i = 0; i < 16; ++i) dst[i] = *(const f32x4*)(wp + (size_t)((krow0) + 2 * i) * ld); } while (0)
; #define P0S_PUT(src, r0) do { _Pragma("unroll") for (int i = 0; i < 16; ++i) { \
;         u32x2 pk; pk.x = cvtpk(src[i][0], src[i][1]) + 0x02800280u; pk.y = cvtpk(src[i][2], src[i][3]) + 0x02800280u;        \
;         *(LAS u32x2*)(img + wb[i & 7] + ((r0) / 16 + (i >> 3)) * 4096) = pk; } } while (0)
; template <int MODE>
; DI void p0_strip_fp8(const float* W, int ld, unsigned char* WT, int K, int n0, LAS unsigned char* img, int lane) {
;     ...
;     P0S_LOAD(va, 0);
; #pragma unroll 1
;     for (int kb = 0; kb < 32; ++kb) {
;         P0S_LOAD(vb, 64 * kb + 32);
;         P0S_PUT(va, 0);
;         if (kb < 31) P0S_LOAD(va, 64 * kb + 64);
;         P0S_PUT(vb, 32);
	v_cvt_pk_bf16_f32 v172, v46, v47
	v_cvt_pk_bf16_f32 v173, v48, v49
	v_add_u32_e32 v172, 0x2800280, v172
	v_add_u32_e32 v173, 0x2800280, v173
	v_cvt_pk_bf16_f32 v166, v20, v21
	ds_write2st64_b64 v165, v[174:175], v[172:173] offset1:8
	s_waitcnt vmcnt(21)
	v_cvt_pk_bf16_f32 v172, v50, v51
	v_cvt_pk_bf16_f32 v173, v52, v53
	v_add_u32_e32 v177, 0x2800280, v166
	v_add_u32_e32 v166, v156, v148
	v_cvt_pk_bf16_f32 v167, v22, v23
	v_add_u32_e32 v172, 0x2800280, v172
	v_add_u32_e32 v173, 0x2800280, v173
	v_add_u32_e32 v178, 0x2800280, v167
	v_cvt_pk_bf16_f32 v167, v24, v25
	ds_write2st64_b64 v166, v[176:177], v[172:173] offset0:2 offset1:10
	s_waitcnt vmcnt(20)
	v_cvt_pk_bf16_f32 v172, v54, v55
	v_cvt_pk_bf16_f32 v173, v56, v57
	v_add_u32_e32 v179, 0x2800280, v167
	v_add_u32_e32 v167, v157, v148
	v_cvt_pk_bf16_f32 v168, v26, v27
	v_add_u32_e32 v172, 0x2800280, v172
	v_add_u32_e32 v173, 0x2800280, v173
	v_add_u32_e32 v180, 0x2800280, v168
	v_cvt_pk_bf16_f32 v168, v28, v29
	ds_write2st64_b64 v167, v[178:179], v[172:173] offset1:8
	s_waitcnt vmcnt(19)
	v_cvt_pk_bf16_f32 v172, v58, v59
	v_cvt_pk_bf16_f32 v173, v60, v61
	v_add_u32_e32 v181, 0x2800280, v168
	v_add_u32_e32 v168, v158, v148
	v_cvt_pk_bf16_f32 v169, v30, v31
	v_add_u32_e32 v172, 0x2800280, v172
	v_add_u32_e32 v173, 0x2800280, v173
	v_add_u32_e32 v182, 0x2800280, v169
	v_cvt_pk_bf16_f32 v169, v32, v33
	ds_write2st64_b64 v168, v[180:181], v[172:173] offset0:4 offset1:12
	s_waitcnt vmcnt(18)
	v_cvt_pk_bf16_f32 v172, v62, v63
	v_cvt_pk_bf16_f32 v173, v64, v65
	v_add_u32_e32 v183, 0x2800280, v169
	v_add_u32_e32 v169, v159, v148
	v_cvt_pk_bf16_f32 v170, v34, v35
	v_add_u32_e32 v172, 0x2800280, v172
	v_add_u32_e32 v173, 0x2800280, v173
	v_add_u32_e32 v184, 0x2800280, v170
	v_cvt_pk_bf16_f32 v170, v36, v37
	ds_write2st64_b64 v169, v[182:183], v[172:173] offset1:8
	s_waitcnt vmcnt(17)
	v_cvt_pk_bf16_f32 v172, v66, v67
	v_cvt_pk_bf16_f32 v173, v68, v69
	v_add_u32_e32 v185, 0x2800280, v170
	v_add_u32_e32 v170, v160, v148
	v_cvt_pk_bf16_f32 v171, v38, v39
	v_add_u32_e32 v172, 0x2800280, v172
	v_add_u32_e32 v173, 0x2800280, v173
	v_add_u32_e32 v186, 0x2800280, v171
	v_cvt_pk_bf16_f32 v171, v40, v41
	ds_write2st64_b64 v170, v[184:185], v[172:173] offset0:6 offset1:14
	s_waitcnt vmcnt(16)
	v_cvt_pk_bf16_f32 v172, v70, v71
	v_cvt_pk_bf16_f32 v173, v72, v73
	v_add_u32_e32 v187, 0x2800280, v171
	v_add_u32_e32 v171, v161, v148
	v_add_u32_e32 v172, 0x2800280, v172
	v_add_u32_e32 v173, 0x2800280, v173
	s_cmp_eq_u32 s62, 31
	ds_write2st64_b64 v171, v[186:187], v[172:173] offset1:8
	s_cbranch_scc1 .LBB0_280
	v_add_co_u32_e32 v10, vcc, 0x80000, v146
	s_nop 1
	v_addc_co_u32_e32 v11, vcc, 0, v147, vcc
	v_add_co_u32_e32 v14, vcc, 0x84000, v146
	s_nop 1
	v_addc_co_u32_e32 v15, vcc, 0, v147, vcc
	v_add_co_u32_e32 v18, vcc, 0x88000, v146
	global_load_dwordx4 v[10:13], v[10:11], off nt
	s_nop 0
	global_load_dwordx4 v[14:17], v[14:15], off nt
	v_addc_co_u32_e32 v19, vcc, 0, v147, vcc
	v_add_co_u32_e32 v22, vcc, 0x8c000, v146
	s_nop 1
	v_addc_co_u32_e32 v23, vcc, 0, v147, vcc
	v_add_co_u32_e32 v26, vcc, 0x90000, v146
	global_load_dwordx4 v[18:21], v[18:19], off nt
	s_nop 0
	global_load_dwordx4 v[22:25], v[22:23], off nt
	v_addc_co_u32_e32 v27, vcc, 0, v147, vcc
	v_add_co_u32_e32 v30, vcc, 0x94000, v146
	s_nop 1
	v_addc_co_u32_e32 v31, vcc, 0, v147, vcc
	v_add_co_u32_e32 v34, vcc, 0x98000, v146
	global_load_dwordx4 v[26:29], v[26:27], off nt
	s_nop 0
	global_load_dwordx4 v[30:33], v[30:31], off nt
	v_addc_co_u32_e32 v35, vcc, 0, v147, vcc
	v_add_co_u32_e32 v38, vcc, 0x9c000, v146
	s_nop 1
	v_addc_co_u32_e32 v39, vcc, 0, v147, vcc
	v_add_co_u32_e32 v42, vcc, 0xa0000, v146
	global_load_dwordx4 v[34:37], v[34:35], off nt
	s_nop 0
	global_load_dwordx4 v[38:41], v[38:39], off nt
	v_addc_co_u32_e32 v43, vcc, 0, v147, vcc
	v_add_co_u32_e32 v46, vcc, 0xa4000, v146
	s_nop 1
	v_addc_co_u32_e32 v47, vcc, 0, v147, vcc
	v_add_co_u32_e32 v50, vcc, 0xa8000, v146
	global_load_dwordx4 v[42:45], v[42:43], off nt
	s_nop 0
	global_load_dwordx4 v[46:49], v[46:47], off nt
	v_addc_co_u32_e32 v51, vcc, 0, v147, vcc
	v_add_co_u32_e32 v54, vcc, 0xac000, v146
	s_nop 1
	v_addc_co_u32_e32 v55, vcc, 0, v147, vcc
	v_add_co_u32_e32 v58, vcc, 0xb0000, v146
	global_load_dwordx4 v[50:53], v[50:51], off nt
	s_nop 0
	global_load_dwordx4 v[54:57], v[54:55], off nt
	v_addc_co_u32_e32 v59, vcc, 0, v147, vcc
	v_add_co_u32_e32 v62, vcc, 0xb4000, v146
	s_nop 1
	v_addc_co_u32_e32 v63, vcc, 0, v147, vcc
	v_add_co_u32_e32 v66, vcc, 0xb8000, v146
	global_load_dwordx4 v[58:61], v[58:59], off nt
	s_nop 0
	global_load_dwordx4 v[62:65], v[62:63], off nt
	v_addc_co_u32_e32 v67, vcc, 0, v147, vcc
	v_add_co_u32_e32 v70, vcc, 0xbc000, v146
	s_nop 1
	v_addc_co_u32_e32 v71, vcc, 0, v147, vcc
	global_load_dwordx4 v[66:69], v[66:67], off nt
	s_nop 0
	global_load_dwordx4 v[70:73], v[70:71], off nt

; DI s16x4 tr16(const LAS unsigned char* p) { return __builtin_bit_cast(s16x4, __builtin_amdgcn_ds_read_tr16_b64_v4i16((LAS v4i16_t*)p)); }
; #define LDS_WAIT() asm volatile("s_waitcnt lgkmcnt(0)" ::: "memory")
; #define P0S_LOAD(dst, krow0) do { _Pragma("unroll") for (int i = 0; i < 16; ++i) dst[i] = *(const f32x4*)(wp + (size_t)((krow0) + 2 * i) * ld); } while (0)
; #define P0S_PUT(src, r0) do { _Pragma("unroll") for (int i = 0; i < 16; ++i) { \
;         u32x2 pk; pk.x = cvtpk(src[i][0], src[i][1]) + 0x02800280u; pk.y = cvtpk(src[i][2], src[i][3]) + 0x02800280u;        \
;         *(LAS u32x2*)(img + wb[i & 7] + ((r0) / 16 + (i >> 3)) * 4096) = pk; } } while (0)
; #define P0S_F8(lo, hi) pk4_fp8m(__uint_as_float((lo) << 16), __uint_as_float((lo) & 0xffff0000u), __uint_as_float((hi) << 16), __uint_as_float((hi) & 0xffff0000u))
; template <int MODE>
; DI void p0_strip_fp8(const float* W, int ld, unsigned char* WT, int K, int n0, LAS unsigned char* img, int lane) {
;     ...
;     P0S_LOAD(va, 0);
; #pragma unroll 1
;     for (int kb = 0; kb < 32; ++kb) {
;         P0S_LOAD(vb, 64 * kb + 32);
;         P0S_PUT(va, 0);
;         if (kb < 31) P0S_LOAD(va, 64 * kb + 64);
;         P0S_PUT(vb, 32);
;         LDS_WAIT();
; #pragma unroll 2
;         for (int nb = 0; nb < 8; ++nb) {
;             const s16x4 t0 = tr16(img + rb[0] + 32 * (nb ^ cx[0])), t1 = tr16(img + rb[1] + 32 * (nb ^ cx[1])), t2 = tr16(img + rb[2] + 32 * (nb ^ cx[2])), t3 = tr16(img + rb[3] + 32 * (nb ^ cx[3]));
;             const u32x2 f0 = __builtin_bit_cast(u32x2, t0), f1 = __builtin_bit_cast(u32x2, t1), f2 = __builtin_bit_cast(u32x2, t2), f3 = __builtin_bit_cast(u32x2, t3);
;             u32x4 o; o.x = P0S_F8(f0.x, f0.y); o.y = P0S_F8(f1.x, f1.y); o.z = P0S_F8(f2.x, f2.y); o.w = P0S_F8(f3.x, f3.y);
;             *(u32x4*)(WT + (size_t)(unsigned)orow[nb] + 64 * kb) = o; }
;         LDS_WAIT();
;     }
.LBB0_281:
	v_xor_b32_e32 v82, s2, v150
	v_xor_b32_e32 v83, s2, v151
	s_cmp_eq_u32 s2, 1
	v_lshlrev_b32_e32 v82, 5, v82
	v_lshlrev_b32_e32 v83, 5, v83
	s_cselect_b64 vcc, -1, 0
	s_cmp_eq_u32 s2, 2
	v_cndmask_b32_e32 v84, v2, v1, vcc
	v_add_u32_e32 v85, v152, v82
	v_add_u32_e32 v86, v153, v82
	v_add_u32_e32 v87, v152, v83
	v_add_u32_e32 v88, v153, v83
	s_cselect_b64 vcc, -1, 0
	s_cmp_eq_u32 s2, 3
	v_cndmask_b32_e32 v90, v84, v4, vcc
	ds_read_b64_tr_b16 v[82:83], v85
	ds_read_b64_tr_b16 v[84:85], v86 offset:1024
	ds_read_b64_tr_b16 v[86:87], v87 offset:2048
	ds_read_b64_tr_b16 v[88:89], v88 offset:3072
	s_cselect_b64 vcc, -1, 0
	s_cmp_eq_u32 s2, 4
	v_cndmask_b32_e32 v90, v90, v3, vcc
	s_cselect_b64 vcc, -1, 0
	s_cmp_eq_u32 s2, 5
	v_cndmask_b32_e32 v90, v90, v6, vcc
	s_cselect_b64 vcc, -1, 0
	s_cmp_eq_u32 s2, 6
	v_cndmask_b32_e32 v90, v90, v5, vcc
	s_cselect_b64 vcc, -1, 0
	s_cmp_eq_u32 s2, 7
	v_cndmask_b32_e32 v90, v90, v8, vcc
	s_cselect_b64 vcc, -1, 0
	s_add_i32 s63, s2, 1
	s_waitcnt lgkmcnt(3)
	v_lshlrev_b32_e32 v91, 16, v82
	v_and_b32_e32 v82, 0xffff0000, v82
	v_lshlrev_b32_e32 v92, 16, v83
	v_and_b32_e32 v83, 0xffff0000, v83
	s_waitcnt lgkmcnt(2)
	v_lshlrev_b32_e32 v93, 16, v84
	v_and_b32_e32 v84, 0xffff0000, v84
	v_lshlrev_b32_e32 v94, 16, v85
	v_and_b32_e32 v85, 0xffff0000, v85
	s_waitcnt lgkmcnt(1)
	v_lshlrev_b32_e32 v95, 16, v86
	v_and_b32_e32 v86, 0xffff0000, v86
	v_lshlrev_b32_e32 v96, 16, v87
	v_and_b32_e32 v87, 0xffff0000, v87
	s_waitcnt lgkmcnt(0)
	v_lshlrev_b32_e32 v97, 16, v88
	v_and_b32_e32 v88, 0xffff0000, v88
	v_lshlrev_b32_e32 v98, 16, v89
	v_and_b32_e32 v89, 0xffff0000, v89
	v_xor_b32_e32 v99, s63, v150
	v_xor_b32_e32 v100, s63, v151
	v_mov_b32_e32 v74, 0
	v_mov_b32_e32 v75, 0
	v_mov_b32_e32 v76, 0
	v_mov_b32_e32 v77, 0
	v_med3_f32 v91, v91, s52, v163
	v_med3_f32 v82, v82, s52, v163
	v_med3_f32 v101, v83, s52, v163
	v_med3_f32 v83, v93, s52, v163
	v_med3_f32 v84, v84, s52, v163
	v_med3_f32 v93, v94, s52, v163
	v_med3_f32 v94, v85, s52, v163
	v_med3_f32 v85, v95, s52, v163
	v_med3_f32 v86, v86, s52, v163
	v_med3_f32 v95, v96, s52, v163
	v_med3_f32 v96, v87, s52, v163
	v_med3_f32 v87, v97, s52, v163
	v_med3_f32 v88, v88, s52, v163
	v_med3_f32 v97, v98, s52, v163
	v_med3_f32 v98, v89, s52, v163
	v_lshlrev_b32_e32 v89, 5, v99
	v_lshlrev_b32_e32 v99, 5, v100
	v_cvt_pk_fp8_f32 v74, v91, v82
	v_cvt_pk_fp8_f32 v75, v83, v84
	v_cvt_pk_fp8_f32 v76, v85, v86
	v_cvt_pk_fp8_f32 v77, v87, v88
	v_add_u32_e32 v82, v152, v89
	v_add_u32_e32 v84, v153, v89
	v_add_u32_e32 v86, v152, v99
	v_add_u32_e32 v88, v153, v99
	ds_read_b64_tr_b16 v[82:83], v82
	ds_read_b64_tr_b16 v[84:85], v84 offset:1024
	ds_read_b64_tr_b16 v[86:87], v86 offset:2048
	ds_read_b64_tr_b16 v[88:89], v88 offset:3072
	v_med3_f32 v92, v92, s52, v163
	s_cmp_eq_u32 s63, 1
	v_cvt_pk_fp8_f32 v74, v92, v101 op_sel:[0,0,1]
	v_cvt_pk_fp8_f32 v75, v93, v94 op_sel:[0,0,1]
	v_cvt_pk_fp8_f32 v76, v95, v96 op_sel:[0,0,1]
	v_cvt_pk_fp8_f32 v77, v97, v98 op_sel:[0,0,1]
	s_waitcnt lgkmcnt(3)
	v_lshlrev_b32_e32 v92, 16, v82
	v_and_b32_e32 v82, 0xffff0000, v82
	s_waitcnt lgkmcnt(2)
	v_lshlrev_b32_e32 v94, 16, v84
	v_and_b32_e32 v84, 0xffff0000, v84
	s_waitcnt lgkmcnt(1)
	v_lshlrev_b32_e32 v96, 16, v86
	v_and_b32_e32 v86, 0xffff0000, v86
	s_waitcnt lgkmcnt(0)
	v_lshlrev_b32_e32 v98, 16, v88
	v_and_b32_e32 v88, 0xffff0000, v88
	v_mov_b32_e32 v78, 0
	v_mov_b32_e32 v79, 0
	v_mov_b32_e32 v80, 0
	v_mov_b32_e32 v81, 0
	v_cndmask_b32_e32 v90, v90, v7, vcc
	s_cselect_b64 vcc, -1, 0
	s_cmp_eq_u32 s63, 2
	v_med3_f32 v92, v92, s52, v163
	v_med3_f32 v82, v82, s52, v163
	v_med3_f32 v94, v94, s52, v163
	v_med3_f32 v84, v84, s52, v163
	v_med3_f32 v96, v96, s52, v163
	v_med3_f32 v86, v86, s52, v163
	v_med3_f32 v98, v98, s52, v163
	v_med3_f32 v88, v88, s52, v163
	v_cndmask_b32_e32 v100, v2, v1, vcc
	s_cselect_b64 vcc, -1, 0
	s_cmp_eq_u32 s63, 3
	v_cvt_pk_fp8_f32 v78, v92, v82
	v_cvt_pk_fp8_f32 v79, v94, v84
	v_cvt_pk_fp8_f32 v80, v96, v86
	v_cvt_pk_fp8_f32 v81, v98, v88
	v_cndmask_b32_e32 v91, v100, v4, vcc
	s_cselect_b64 vcc, -1, 0
	s_cmp_eq_u32 s63, 4
	v_cndmask_b32_e32 v91, v91, v3, vcc
	s_cselect_b64 vcc, -1, 0
	s_cmp_eq_u32 s63, 5
	v_lshlrev_b32_e32 v93, 16, v83
	v_and_b32_e32 v83, 0xffff0000, v83
	v_lshlrev_b32_e32 v95, 16, v85
	v_and_b32_e32 v85, 0xffff0000, v85
	v_lshlrev_b32_e32 v97, 16, v87
	v_and_b32_e32 v87, 0xffff0000, v87
	v_lshlrev_b32_e32 v99, 16, v89
	v_and_b32_e32 v89, 0xffff0000, v89
	v_cndmask_b32_e32 v91, v91, v6, vcc
	s_cselect_b64 vcc, -1, 0
	s_cmp_eq_u32 s63, 6
	v_med3_f32 v93, v93, s52, v163
	v_med3_f32 v83, v83, s52, v163
	v_med3_f32 v95, v95, s52, v163
	v_med3_f32 v85, v85, s52, v163
	v_med3_f32 v97, v97, s52, v163
	v_med3_f32 v87, v87, s52, v163
	v_med3_f32 v99, v99, s52, v163
	v_med3_f32 v89, v89, s52, v163
	v_cndmask_b32_e32 v91, v91, v5, vcc
	s_cselect_b64 vcc, -1, 0
	s_cmp_eq_u32 s63, 7
	v_cvt_pk_fp8_f32 v78, v93, v83 op_sel:[0,0,1]
	v_cvt_pk_fp8_f32 v79, v95, v85 op_sel:[0,0,1]
	v_cvt_pk_fp8_f32 v80, v97, v87 op_sel:[0,0,1]
	v_cvt_pk_fp8_f32 v81, v99, v89 op_sel:[0,0,1]
	v_cndmask_b32_e32 v91, v91, v8, vcc
	s_cselect_b64 vcc, -1, 0
	s_add_i32 s2, s2, 2
	s_cmp_eq_u32 s2, 8
	v_cndmask_b32_e32 v91, v91, v7, vcc
	global_store_dwordx4 v90, v[74:77], s[6:7] nt
	global_store_dwordx4 v91, v[78:81], s[6:7] nt
	s_cbranch_scc0 .LBB0_281
	s_sleep 30
	s_waitcnt lgkmcnt(0)
	s_add_i32 s62, s62, 1
	s_cmp_eq_u32 s62, 32
	s_cbranch_scc0 .LBB0_278
	s_mov_b64 s[0:1], 0
; #define P0S_LOAD(dst, krow0) do { _Pragma("unroll") for (int i = 0; i < 16; ++i) dst[i] = *(const f32x4*)(wp + (size_t)((krow0) + 2 * i) * ld); } while (0)
; #define P0S_PUT(src, r0) do { _Pragma("unroll") for (int i = 0; i < 16; ++i) { \
;         u32x2 pk; pk.x = cvtpk(src[i][0], src[i][1]) + 0x02800280u; pk.y = cvtpk(src[i][2], src[i][3]) + 0x02800280u;        \
;         *(LAS u32x2*)(img + wb[i & 7] + ((r0) / 16 + (i >> 3)) * 4096) = pk; } } while (0)
; template <int MODE>
; DI void p0_strip_fp8(const float* W, int ld, unsigned char* WT, int K, int n0, LAS unsigned char* img, int lane) {
;     ...
;     for (int nb = 0; nb < 8; ++nb) { const int n = n0 + 16 * nb + i16; int row = n; if (MODE == 1) { const int ff = n >> 1; row = 256 * (ff >> 7) + 128 * (n & 1) + (ff & 127); } orow[nb] = row * K + 16 * g; }
;     f32x4 va[16], vb[16];
;     ...
;     P0S_LOAD(va, 0);
; #pragma unroll 1
;     for (int kb = 0; kb < 32; ++kb) {
;         P0S_LOAD(vb, 64 * kb + 32);
;         P0S_PUT(va, 0);
;         if (kb < 31) P0S_LOAD(va, 64 * kb + 64);
;         P0S_PUT(vb, 32);
; DI void p0_expert_weights(Frame& F, int wk, int nwk) {
;     ...
;         if (cx < C_UP) { const int e = cx >> 5, nb = cx & 31; p0_strip_fp8<1>(F.w_up + (size_t)e * DM * UPW, UPW, F.ws + WS_WUP + (size_t)e * UPW * DM, DM, 128 * nb, img, F.lane); }
.LBB0_284:
	s_and_b64 vcc, exec, s[0:1]
	s_cbranch_vccz .LBB0_275
	s_ashr_i32 s0, s8, 5
	s_ashr_i32 s1, s0, 31
	s_lshl_b64 s[6:7], s[0:1], 25
	s_lshl_b64 s[0:1], s[0:1], 23
	s_add_u32 s0, s11, s0
	s_addc_u32 s1, s14, s1
	s_and_b32 s2, s61, 0xf80
	v_lshl_add_u64 v[2:3], v[142:143], 0, s[6:7]
	s_lshl_b32 s2, s2, 2
	v_lshl_add_u64 v[2:3], v[2:3], 0, s[2:3]
	v_lshl_add_u64 v[144:145], v[2:3], 0, v[138:139]
	v_add_co_u32_e32 v2, vcc, s15, v144
	v_or_b32_e32 v1, s61, v9
	s_nop 0
	v_addc_co_u32_e32 v3, vcc, 0, v145, vcc
	global_load_dwordx4 v[10:13], v[144:145], off nt
	global_load_dwordx4 v[14:17], v[2:3], off nt
	v_add_co_u32_e32 v2, vcc, s16, v144
	v_lshrrev_b32_e32 v1, 1, v1
	s_nop 0
	v_addc_co_u32_e32 v3, vcc, 0, v145, vcc
	v_add_co_u32_e32 v4, vcc, s17, v144
	s_and_b32 s2, s61, 0xf00
	s_nop 0
	v_addc_co_u32_e32 v5, vcc, 0, v145, vcc
	global_load_dwordx4 v[18:21], v[2:3], off nt
	global_load_dwordx4 v[22:25], v[4:5], off nt
	v_add_co_u32_e32 v2, vcc, s18, v144
	v_and_b32_e32 v1, 0x47, v1
	s_nop 0
	v_addc_co_u32_e32 v3, vcc, 0, v145, vcc
	v_add_co_u32_e32 v4, vcc, s19, v144
	v_or3_b32 v1, s2, v162, v1
	s_nop 0
	v_addc_co_u32_e32 v5, vcc, 0, v145, vcc
	global_load_dwordx4 v[26:29], v[2:3], off nt
	global_load_dwordx4 v[30:33], v[4:5], off nt
	v_add_co_u32_e32 v2, vcc, s20, v144
	s_mov_b32 s61, 0
	s_nop 0
	v_addc_co_u32_e32 v3, vcc, 0, v145, vcc
	v_add_co_u32_e32 v4, vcc, s21, v144
	s_nop 1
	v_addc_co_u32_e32 v5, vcc, 0, v145, vcc
	global_load_dwordx4 v[34:37], v[2:3], off nt
	global_load_dwordx4 v[38:41], v[4:5], off nt
	v_add_co_u32_e32 v2, vcc, s27, v144
	s_nop 1
	v_addc_co_u32_e32 v3, vcc, 0, v145, vcc
	v_add_co_u32_e32 v4, vcc, s29, v144
	s_nop 1
	v_addc_co_u32_e32 v5, vcc, 0, v145, vcc
	global_load_dwordx4 v[42:45], v[2:3], off nt
	global_load_dwordx4 v[46:49], v[4:5], off nt
	v_add_co_u32_e32 v2, vcc, s31, v144
	s_nop 1
	v_addc_co_u32_e32 v3, vcc, 0, v145, vcc
	v_add_co_u32_e32 v4, vcc, s34, v144
	s_nop 1
	v_addc_co_u32_e32 v5, vcc, 0, v145, vcc
	global_load_dwordx4 v[50:53], v[2:3], off nt
	global_load_dwordx4 v[54:57], v[4:5], off nt
	v_add_co_u32_e32 v2, vcc, s36, v144
	s_nop 1
	v_addc_co_u32_e32 v3, vcc, 0, v145, vcc
	v_add_co_u32_e32 v4, vcc, 0x68000, v144
	s_nop 1
	v_addc_co_u32_e32 v5, vcc, 0, v145, vcc
	global_load_dwordx4 v[58:61], v[2:3], off nt
	global_load_dwordx4 v[62:65], v[4:5], off nt
	v_add_co_u32_e32 v2, vcc, 0x70000, v144
	s_nop 1
	v_addc_co_u32_e32 v3, vcc, 0, v145, vcc
	v_add_co_u32_e32 v4, vcc, 0x78000, v144
	s_nop 1
	v_addc_co_u32_e32 v5, vcc, 0, v145, vcc
	global_load_dwordx4 v[66:69], v[2:3], off nt
	global_load_dwordx4 v[70:73], v[4:5], off nt
	v_lshl_or_b32 v2, v1, 11, v149
	v_or_b32_e32 v1, 0x4000, v2
	v_or_b32_e32 v4, 0x8000, v2
	v_or_b32_e32 v3, 0xc000, v2
	v_or_b32_e32 v6, 0x10000, v2
	v_or_b32_e32 v5, 0x14000, v2
	v_or_b32_e32 v8, 0x18000, v2
	v_or_b32_e32 v7, 0x1c000, v2
.LBB0_286:
	s_lshl_b32 s2, s61, 18
	v_lshl_add_u64 v[146:147], s[2:3], 2, v[144:145]
	s_waitcnt vmcnt(26)
	v_add_co_u32_e32 v74, vcc, s44, v146
	s_waitcnt vmcnt(15)
	v_cvt_pk_bf16_f32 v164, v10, v11
	v_addc_co_u32_e32 v75, vcc, 0, v147, vcc
	v_add_co_u32_e32 v76, vcc, s45, v146
	v_add_u32_e32 v172, 0x2800280, v164
	s_nop 0
	v_addc_co_u32_e32 v77, vcc, 0, v147, vcc
	global_load_dwordx4 v[134:137], v[74:75], off nt
	global_load_dwordx4 v[118:121], v[76:77], off nt
	v_add_co_u32_e32 v74, vcc, s46, v146
	v_cvt_pk_bf16_f32 v164, v12, v13
	s_nop 0
	v_addc_co_u32_e32 v75, vcc, 0, v147, vcc
	v_add_co_u32_e32 v76, vcc, s47, v146
	s_waitcnt vmcnt(9)
	v_cvt_pk_bf16_f32 v188, v42, v43
	v_addc_co_u32_e32 v77, vcc, 0, v147, vcc
	global_load_dwordx4 v[130:133], v[74:75], off nt
	global_load_dwordx4 v[110:113], v[76:77], off nt
	v_add_co_u32_e32 v74, vcc, s48, v146
	v_cvt_pk_bf16_f32 v189, v44, v45
	s_nop 0
	v_addc_co_u32_e32 v75, vcc, 0, v147, vcc
	v_add_co_u32_e32 v76, vcc, s49, v146
	v_add_u32_e32 v173, 0x2800280, v164
	s_nop 0
	v_addc_co_u32_e32 v77, vcc, 0, v147, vcc
	global_load_dwordx4 v[126:129], v[74:75], off nt
	global_load_dwordx4 v[106:109], v[76:77], off nt
	v_add_co_u32_e32 v74, vcc, s50, v146
	v_add_u32_e32 v164, v154, v148
	s_nop 0
	v_addc_co_u32_e32 v75, vcc, 0, v147, vcc
	v_add_co_u32_e32 v76, vcc, s51, v146
	v_cvt_pk_bf16_f32 v165, v14, v15
	s_nop 0
	v_addc_co_u32_e32 v77, vcc, 0, v147, vcc
	global_load_dwordx4 v[122:125], v[74:75], off nt
	global_load_dwordx4 v[102:105], v[76:77], off nt
	v_add_co_u32_e32 v74, vcc, s53, v146
	v_add_u32_e32 v188, 0x2800280, v188
	s_nop 0
	v_addc_co_u32_e32 v75, vcc, 0, v147, vcc
	v_add_co_u32_e32 v76, vcc, s54, v146
	v_add_u32_e32 v189, 0x2800280, v189
	s_nop 0
	v_addc_co_u32_e32 v77, vcc, 0, v147, vcc
	global_load_dwordx4 v[114:117], v[74:75], off nt
	global_load_dwordx4 v[94:97], v[76:77], off nt
	v_add_co_u32_e32 v74, vcc, s55, v146
	v_add_u32_e32 v174, 0x2800280, v165
	s_nop 0
	v_addc_co_u32_e32 v75, vcc, 0, v147, vcc
	v_add_co_u32_e32 v76, vcc, s56, v146
	v_cvt_pk_bf16_f32 v165, v16, v17
	s_nop 0
	v_addc_co_u32_e32 v77, vcc, 0, v147, vcc
	global_load_dwordx4 v[98:101], v[74:75], off nt
	global_load_dwordx4 v[86:89], v[76:77], off nt
	v_add_co_u32_e32 v74, vcc, s57, v146
	v_add_u32_e32 v175, 0x2800280, v165
	s_nop 0
	v_addc_co_u32_e32 v75, vcc, 0, v147, vcc
	v_add_co_u32_e32 v76, vcc, s58, v146
	v_add_u32_e32 v165, v155, v148
	s_nop 0
	v_addc_co_u32_e32 v77, vcc, 0, v147, vcc
	global_load_dwordx4 v[90:93], v[74:75], off nt
	global_load_dwordx4 v[78:81], v[76:77], off nt
	v_add_co_u32_e32 v74, vcc, s59, v146
	v_cvt_pk_bf16_f32 v166, v18, v19
	s_nop 0
	v_addc_co_u32_e32 v75, vcc, 0, v147, vcc
	v_add_co_u32_e32 v76, vcc, s60, v146
	v_add_u32_e32 v176, 0x2800280, v166
	s_nop 0
	v_addc_co_u32_e32 v77, vcc, 0, v147, vcc
	global_load_dwordx4 v[82:85], v[74:75], off nt
	s_nop 0
	global_load_dwordx4 v[74:77], v[76:77], off nt
	ds_write2st64_b64 v164, v[172:173], v[188:189] offset1:8
	s_waitcnt vmcnt(22)
; #define P0S_LOAD(dst, krow0) do { _Pragma("unroll") for (int i = 0; i < 16; ++i) dst[i] = *(const f32x4*)(wp + (size_t)((krow0) + 2 * i) * ld); } while (0)
; #define P0S_PUT(src, r0) do { _Pragma("unroll") for (int i = 0; i < 16; ++i) { \
;         u32x2 pk; pk.x = cvtpk(src[i][0], src[i][1]) + 0x02800280u; pk.y = cvtpk(src[i][2], src[i][3]) + 0x02800280u;        \
;         *(LAS u32x2*)(img + wb[i & 7] + ((r0) / 16 + (i >> 3)) * 4096) = pk; } } while (0)
; template <int MODE>
; DI void p0_strip_fp8(const float* W, int ld, unsigned char* WT, int K, int n0, LAS unsigned char* img, int lane) {
;     ...
;     P0S_LOAD(va, 0);
; #pragma unroll 1
;     for (int kb = 0; kb < 32; ++kb) {
;         P0S_LOAD(vb, 64 * kb + 32);
;         P0S_PUT(va, 0);
;         if (kb < 31) P0S_LOAD(va, 64 * kb + 64);
;         P0S_PUT(vb, 32);
	v_cvt_pk_bf16_f32 v172, v46, v47
	v_cvt_pk_bf16_f32 v173, v48, v49
	v_add_u32_e32 v172, 0x2800280, v172
	v_add_u32_e32 v173, 0x2800280, v173
	v_cvt_pk_bf16_f32 v166, v20, v21
	ds_write2st64_b64 v165, v[174:175], v[172:173] offset1:8
	s_waitcnt vmcnt(21)
	v_cvt_pk_bf16_f32 v172, v50, v51
	v_cvt_pk_bf16_f32 v173, v52, v53
	v_add_u32_e32 v177, 0x2800280, v166
	v_add_u32_e32 v166, v156, v148
	v_cvt_pk_bf16_f32 v167, v22, v23
	v_add_u32_e32 v172, 0x2800280, v172
	v_add_u32_e32 v173, 0x2800280, v173
	v_add_u32_e32 v178, 0x2800280, v167
	v_cvt_pk_bf16_f32 v167, v24, v25
	ds_write2st64_b64 v166, v[176:177], v[172:173] offset0:2 offset1:10
	s_waitcnt vmcnt(20)
	v_cvt_pk_bf16_f32 v172, v54, v55
	v_cvt_pk_bf16_f32 v173, v56, v57
	v_add_u32_e32 v179, 0x2800280, v167
	v_add_u32_e32 v167, v157, v148
	v_cvt_pk_bf16_f32 v168, v26, v27
	v_add_u32_e32 v172, 0x2800280, v172
	v_add_u32_e32 v173, 0x2800280, v173
	v_add_u32_e32 v180, 0x2800280, v168
	v_cvt_pk_bf16_f32 v168, v28, v29
	ds_write2st64_b64 v167, v[178:179], v[172:173] offset1:8
	s_waitcnt vmcnt(19)
	v_cvt_pk_bf16_f32 v172, v58, v59
	v_cvt_pk_bf16_f32 v173, v60, v61
	v_add_u32_e32 v181, 0x2800280, v168
	v_add_u32_e32 v168, v158, v148
	v_cvt_pk_bf16_f32 v169, v30, v31
	v_add_u32_e32 v172, 0x2800280, v172
	v_add_u32_e32 v173, 0x2800280, v173
	v_add_u32_e32 v182, 0x2800280, v169
	v_cvt_pk_bf16_f32 v169, v32, v33
	ds_write2st64_b64 v168, v[180:181], v[172:173] offset0:4 offset1:12
	s_waitcnt vmcnt(18)
	v_cvt_pk_bf16_f32 v172, v62, v63
	v_cvt_pk_bf16_f32 v173, v64, v65
	v_add_u32_e32 v183, 0x2800280, v169
	v_add_u32_e32 v169, v159, v148
	v_cvt_pk_bf16_f32 v170, v34, v35
	v_add_u32_e32 v172, 0x2800280, v172
	v_add_u32_e32 v173, 0x2800280, v173
	v_add_u32_e32 v184, 0x2800280, v170
	v_cvt_pk_bf16_f32 v170, v36, v37
	ds_write2st64_b64 v169, v[182:183], v[172:173] offset1:8
	s_waitcnt vmcnt(17)
	v_cvt_pk_bf16_f32 v172, v66, v67
	v_cvt_pk_bf16_f32 v173, v68, v69
	v_add_u32_e32 v185, 0x2800280, v170
	v_add_u32_e32 v170, v160, v148
	v_cvt_pk_bf16_f32 v171, v38, v39
	v_add_u32_e32 v172, 0x2800280, v172
	v_add_u32_e32 v173, 0x2800280, v173
	v_add_u32_e32 v186, 0x2800280, v171
	v_cvt_pk_bf16_f32 v171, v40, v41
	ds_write2st64_b64 v170, v[184:185], v[172:173] offset0:6 offset1:14
	s_waitcnt vmcnt(16)
	v_cvt_pk_bf16_f32 v172, v70, v71
	v_cvt_pk_bf16_f32 v173, v72, v73
	v_add_u32_e32 v187, 0x2800280, v171
	v_add_u32_e32 v171, v161, v148
	v_add_u32_e32 v172, 0x2800280, v172
	v_add_u32_e32 v173, 0x2800280, v173
	s_cmp_eq_u32 s61, 31
	ds_write2st64_b64 v171, v[186:187], v[172:173] offset1:8
	s_cbranch_scc1 .LBB0_288
	v_add_co_u32_e32 v10, vcc, 0x100000, v146
	s_nop 1
	v_addc_co_u32_e32 v11, vcc, 0, v147, vcc
	v_add_co_u32_e32 v14, vcc, 0x108000, v146
	s_nop 1
	v_addc_co_u32_e32 v15, vcc, 0, v147, vcc
	v_add_co_u32_e32 v18, vcc, 0x110000, v146
	global_load_dwordx4 v[10:13], v[10:11], off nt
	s_nop 0
	global_load_dwordx4 v[14:17], v[14:15], off nt
	v_addc_co_u32_e32 v19, vcc, 0, v147, vcc
	v_add_co_u32_e32 v22, vcc, 0x118000, v146
	s_nop 1
	v_addc_co_u32_e32 v23, vcc, 0, v147, vcc
	v_add_co_u32_e32 v26, vcc, 0x120000, v146
	global_load_dwordx4 v[18:21], v[18:19], off nt
	s_nop 0
	global_load_dwordx4 v[22:25], v[22:23], off nt
	v_addc_co_u32_e32 v27, vcc, 0, v147, vcc
	v_add_co_u32_e32 v30, vcc, 0x128000, v146
	s_nop 1
	v_addc_co_u32_e32 v31, vcc, 0, v147, vcc
	v_add_co_u32_e32 v34, vcc, 0x130000, v146
	global_load_dwordx4 v[26:29], v[26:27], off nt
	s_nop 0
	global_load_dwordx4 v[30:33], v[30:31], off nt
	v_addc_co_u32_e32 v35, vcc, 0, v147, vcc
	v_add_co_u32_e32 v38, vcc, 0x138000, v146
	s_nop 1
	v_addc_co_u32_e32 v39, vcc, 0, v147, vcc
	v_add_co_u32_e32 v42, vcc, 0x140000, v146
	global_load_dwordx4 v[34:37], v[34:35], off nt
	s_nop 0
	global_load_dwordx4 v[38:41], v[38:39], off nt
	v_addc_co_u32_e32 v43, vcc, 0, v147, vcc
	v_add_co_u32_e32 v46, vcc, 0x148000, v146
	s_nop 1
	v_addc_co_u32_e32 v47, vcc, 0, v147, vcc
	v_add_co_u32_e32 v50, vcc, 0x150000, v146
	global_load_dwordx4 v[42:45], v[42:43], off nt
	s_nop 0
	global_load_dwordx4 v[46:49], v[46:47], off nt
	v_addc_co_u32_e32 v51, vcc, 0, v147, vcc
	v_add_co_u32_e32 v54, vcc, 0x158000, v146
	s_nop 1
	v_addc_co_u32_e32 v55, vcc, 0, v147, vcc
	v_add_co_u32_e32 v58, vcc, 0x160000, v146
	global_load_dwordx4 v[50:53], v[50:51], off nt
	s_nop 0
	global_load_dwordx4 v[54:57], v[54:55], off nt
	v_addc_co_u32_e32 v59, vcc, 0, v147, vcc
	v_add_co_u32_e32 v62, vcc, 0x168000, v146
	s_nop 1
	v_addc_co_u32_e32 v63, vcc, 0, v147, vcc
	v_add_co_u32_e32 v66, vcc, 0x170000, v146
	global_load_dwordx4 v[58:61], v[58:59], off nt
	s_nop 0
	global_load_dwordx4 v[62:65], v[62:63], off nt
	v_addc_co_u32_e32 v67, vcc, 0, v147, vcc
	v_add_co_u32_e32 v70, vcc, 0x178000, v146
	s_nop 1
	v_addc_co_u32_e32 v71, vcc, 0, v147, vcc
	global_load_dwordx4 v[66:69], v[66:67], off nt
	s_nop 0
	global_load_dwordx4 v[70:73], v[70:71], off nt

; DI s16x4 tr16(const LAS unsigned char* p) { return __builtin_bit_cast(s16x4, __builtin_amdgcn_ds_read_tr16_b64_v4i16((LAS v4i16_t*)p)); }
; #define LDS_WAIT() asm volatile("s_waitcnt lgkmcnt(0)" ::: "memory")
; #define P0S_LOAD(dst, krow0) do { _Pragma("unroll") for (int i = 0; i < 16; ++i) dst[i] = *(const f32x4*)(wp + (size_t)((krow0) + 2 * i) * ld); } while (0)
; #define P0S_PUT(src, r0) do { _Pragma("unroll") for (int i = 0; i < 16; ++i) { \
;         u32x2 pk; pk.x = cvtpk(src[i][0], src[i][1]) + 0x02800280u; pk.y = cvtpk(src[i][2], src[i][3]) + 0x02800280u;        \
;         *(LAS u32x2*)(img + wb[i & 7] + ((r0) / 16 + (i >> 3)) * 4096) = pk; } } while (0)
; #define P0S_F8(lo, hi) pk4_fp8m(__uint_as_float((lo) << 16), __uint_as_float((lo) & 0xffff0000u), __uint_as_float((hi) << 16), __uint_as_float((hi) & 0xffff0000u))
; template <int MODE>
; DI void p0_strip_fp8(const float* W, int ld, unsigned char* WT, int K, int n0, LAS unsigned char* img, int lane) {
;     ...
;     P0S_LOAD(va, 0);
; #pragma unroll 1
;     for (int kb = 0; kb < 32; ++kb) {
;         P0S_LOAD(vb, 64 * kb + 32);
;         P0S_PUT(va, 0);
;         if (kb < 31) P0S_LOAD(va, 64 * kb + 64);
;         P0S_PUT(vb, 32);
;         LDS_WAIT();
; #pragma unroll 2
;         for (int nb = 0; nb < 8; ++nb) {
;             const s16x4 t0 = tr16(img + rb[0] + 32 * (nb ^ cx[0])), t1 = tr16(img + rb[1] + 32 * (nb ^ cx[1])), t2 = tr16(img + rb[2] + 32 * (nb ^ cx[2])), t3 = tr16(img + rb[3] + 32 * (nb ^ cx[3]));
;             const u32x2 f0 = __builtin_bit_cast(u32x2, t0), f1 = __builtin_bit_cast(u32x2, t1), f2 = __builtin_bit_cast(u32x2, t2), f3 = __builtin_bit_cast(u32x2, t3);
;             u32x4 o; o.x = P0S_F8(f0.x, f0.y); o.y = P0S_F8(f1.x, f1.y); o.z = P0S_F8(f2.x, f2.y); o.w = P0S_F8(f3.x, f3.y);
;             *(u32x4*)(WT + (size_t)(unsigned)orow[nb] + 64 * kb) = o; }
;         LDS_WAIT();
;     }
.LBB0_289:
	v_xor_b32_e32 v82, s2, v150
	v_xor_b32_e32 v83, s2, v151
	s_cmp_eq_u32 s2, 1
	v_lshlrev_b32_e32 v82, 5, v82
	v_lshlrev_b32_e32 v83, 5, v83
	s_cselect_b64 vcc, -1, 0
	s_cmp_eq_u32 s2, 2
	v_cndmask_b32_e32 v84, v2, v1, vcc
	v_add_u32_e32 v85, v152, v82
	v_add_u32_e32 v86, v153, v82
	v_add_u32_e32 v87, v152, v83
	v_add_u32_e32 v88, v153, v83
	s_cselect_b64 vcc, -1, 0
	s_cmp_eq_u32 s2, 3
	v_cndmask_b32_e32 v90, v84, v4, vcc
	ds_read_b64_tr_b16 v[82:83], v85
	ds_read_b64_tr_b16 v[84:85], v86 offset:1024
	ds_read_b64_tr_b16 v[86:87], v87 offset:2048
	ds_read_b64_tr_b16 v[88:89], v88 offset:3072
	s_cselect_b64 vcc, -1, 0
	s_cmp_eq_u32 s2, 4
	v_cndmask_b32_e32 v90, v90, v3, vcc
	s_cselect_b64 vcc, -1, 0
	s_cmp_eq_u32 s2, 5
	v_cndmask_b32_e32 v90, v90, v6, vcc
	s_cselect_b64 vcc, -1, 0
	s_cmp_eq_u32 s2, 6
	v_cndmask_b32_e32 v90, v90, v5, vcc
	s_cselect_b64 vcc, -1, 0
	s_cmp_eq_u32 s2, 7
	v_cndmask_b32_e32 v90, v90, v8, vcc
	s_cselect_b64 vcc, -1, 0
	s_add_i32 s62, s2, 1
	s_waitcnt lgkmcnt(3)
	v_lshlrev_b32_e32 v91, 16, v82
	v_and_b32_e32 v82, 0xffff0000, v82
	v_lshlrev_b32_e32 v92, 16, v83
	v_and_b32_e32 v83, 0xffff0000, v83
	s_waitcnt lgkmcnt(2)
	v_lshlrev_b32_e32 v93, 16, v84
	v_and_b32_e32 v84, 0xffff0000, v84
	v_lshlrev_b32_e32 v94, 16, v85
	v_and_b32_e32 v85, 0xffff0000, v85
	s_waitcnt lgkmcnt(1)
	v_lshlrev_b32_e32 v95, 16, v86
	v_and_b32_e32 v86, 0xffff0000, v86
	v_lshlrev_b32_e32 v96, 16, v87
	v_and_b32_e32 v87, 0xffff0000, v87
	s_waitcnt lgkmcnt(0)
	v_lshlrev_b32_e32 v97, 16, v88
	v_and_b32_e32 v88, 0xffff0000, v88
	v_lshlrev_b32_e32 v98, 16, v89
	v_and_b32_e32 v89, 0xffff0000, v89
	v_xor_b32_e32 v99, s62, v150
	v_xor_b32_e32 v100, s62, v151
	v_mov_b32_e32 v74, 0
	v_mov_b32_e32 v75, 0
	v_mov_b32_e32 v76, 0
	v_mov_b32_e32 v77, 0
	v_med3_f32 v91, v91, s52, v163
	v_med3_f32 v82, v82, s52, v163
	v_med3_f32 v101, v83, s52, v163
	v_med3_f32 v83, v93, s52, v163
	v_med3_f32 v84, v84, s52, v163
	v_med3_f32 v93, v94, s52, v163
	v_med3_f32 v94, v85, s52, v163
	v_med3_f32 v85, v95, s52, v163
	v_med3_f32 v86, v86, s52, v163
	v_med3_f32 v95, v96, s52, v163
	v_med3_f32 v96, v87, s52, v163
	v_med3_f32 v87, v97, s52, v163
	v_med3_f32 v88, v88, s52, v163
	v_med3_f32 v97, v98, s52, v163
	v_med3_f32 v98, v89, s52, v163
	v_lshlrev_b32_e32 v89, 5, v99
	v_lshlrev_b32_e32 v99, 5, v100
	v_cvt_pk_fp8_f32 v74, v91, v82
	v_cvt_pk_fp8_f32 v75, v83, v84
	v_cvt_pk_fp8_f32 v76, v85, v86
	v_cvt_pk_fp8_f32 v77, v87, v88
	v_add_u32_e32 v82, v152, v89
	v_add_u32_e32 v84, v153, v89
	v_add_u32_e32 v86, v152, v99
	v_add_u32_e32 v88, v153, v99
	ds_read_b64_tr_b16 v[82:83], v82
	ds_read_b64_tr_b16 v[84:85], v84 offset:1024
	ds_read_b64_tr_b16 v[86:87], v86 offset:2048
	ds_read_b64_tr_b16 v[88:89], v88 offset:3072
	v_med3_f32 v92, v92, s52, v163
	s_cmp_eq_u32 s62, 1
	v_cvt_pk_fp8_f32 v74, v92, v101 op_sel:[0,0,1]
	v_cvt_pk_fp8_f32 v75, v93, v94 op_sel:[0,0,1]
	v_cvt_pk_fp8_f32 v76, v95, v96 op_sel:[0,0,1]
	v_cvt_pk_fp8_f32 v77, v97, v98 op_sel:[0,0,1]
	s_waitcnt lgkmcnt(3)
	v_lshlrev_b32_e32 v92, 16, v82
	v_and_b32_e32 v82, 0xffff0000, v82
	s_waitcnt lgkmcnt(2)
	v_lshlrev_b32_e32 v94, 16, v84
	v_and_b32_e32 v84, 0xffff0000, v84
	s_waitcnt lgkmcnt(1)
	v_lshlrev_b32_e32 v96, 16, v86
	v_and_b32_e32 v86, 0xffff0000, v86
	s_waitcnt lgkmcnt(0)
	v_lshlrev_b32_e32 v98, 16, v88
	v_and_b32_e32 v88, 0xffff0000, v88
	v_mov_b32_e32 v78, 0
	v_mov_b32_e32 v79, 0
	v_mov_b32_e32 v80, 0
	v_mov_b32_e32 v81, 0
	v_cndmask_b32_e32 v90, v90, v7, vcc
	s_cselect_b64 vcc, -1, 0
	s_cmp_eq_u32 s62, 2
	v_med3_f32 v92, v92, s52, v163
	v_med3_f32 v82, v82, s52, v163
	v_med3_f32 v94, v94, s52, v163
	v_med3_f32 v84, v84, s52, v163
	v_med3_f32 v96, v96, s52, v163
	v_med3_f32 v86, v86, s52, v163
	v_med3_f32 v98, v98, s52, v163
	v_med3_f32 v88, v88, s52, v163
	v_cndmask_b32_e32 v100, v2, v1, vcc
	s_cselect_b64 vcc, -1, 0
	s_cmp_eq_u32 s62, 3
	v_cvt_pk_fp8_f32 v78, v92, v82
	v_cvt_pk_fp8_f32 v79, v94, v84
	v_cvt_pk_fp8_f32 v80, v96, v86
	v_cvt_pk_fp8_f32 v81, v98, v88
	v_cndmask_b32_e32 v91, v100, v4, vcc
	s_cselect_b64 vcc, -1, 0
	s_cmp_eq_u32 s62, 4
	v_cndmask_b32_e32 v91, v91, v3, vcc
	s_cselect_b64 vcc, -1, 0
	s_cmp_eq_u32 s62, 5
	v_lshlrev_b32_e32 v93, 16, v83
	v_and_b32_e32 v83, 0xffff0000, v83
	v_lshlrev_b32_e32 v95, 16, v85
	v_and_b32_e32 v85, 0xffff0000, v85
	v_lshlrev_b32_e32 v97, 16, v87
	v_and_b32_e32 v87, 0xffff0000, v87
	v_lshlrev_b32_e32 v99, 16, v89
	v_and_b32_e32 v89, 0xffff0000, v89
	v_cndmask_b32_e32 v91, v91, v6, vcc
	s_cselect_b64 vcc, -1, 0
	s_cmp_eq_u32 s62, 6
	v_med3_f32 v93, v93, s52, v163
	v_med3_f32 v83, v83, s52, v163
	v_med3_f32 v95, v95, s52, v163
	v_med3_f32 v85, v85, s52, v163
	v_med3_f32 v97, v97, s52, v163
	v_med3_f32 v87, v87, s52, v163
	v_med3_f32 v99, v99, s52, v163
	v_med3_f32 v89, v89, s52, v163
	v_cndmask_b32_e32 v91, v91, v5, vcc
	s_cselect_b64 vcc, -1, 0
	s_cmp_eq_u32 s62, 7
	v_cvt_pk_fp8_f32 v78, v93, v83 op_sel:[0,0,1]
	v_cvt_pk_fp8_f32 v79, v95, v85 op_sel:[0,0,1]
	v_cvt_pk_fp8_f32 v80, v97, v87 op_sel:[0,0,1]
	v_cvt_pk_fp8_f32 v81, v99, v89 op_sel:[0,0,1]
	v_cndmask_b32_e32 v91, v91, v8, vcc
	s_cselect_b64 vcc, -1, 0
	s_add_i32 s2, s2, 2
	s_cmp_eq_u32 s2, 8
	v_cndmask_b32_e32 v91, v91, v7, vcc
	global_store_dwordx4 v90, v[74:77], s[6:7] nt
	global_store_dwordx4 v91, v[78:81], s[6:7] nt
	s_cbranch_scc0 .LBB0_289
	s_sleep 30
	s_waitcnt lgkmcnt(0)
	s_add_i32 s61, s61, 1
	s_cmp_eq_u32 s61, 32
	s_cbranch_scc0 .LBB0_286
	s_branch .LBB0_275
